# attention: previous tile's row-sum/exp/bf16-pack VALU head moved into the MFMA shadow of the current tile's QK^T burst (lever: MFMA-VALU interleave across segments)
# baseline (speedup 1.0000x reference)
.LBB0_3234:
	s_waitcnt vmcnt(0)
	ds_read_b128 v[178:181], v198 offset:49152
	ds_read_b128 v[216:219], v198 offset:57344
	ds_read_b128 v[228:231], v204 offset:49152
	ds_read_b128 v[232:235], v204 offset:57344
	ds_read_b128 v[238:241], v205 offset:49152
	ds_read_b128 v[242:245], v205 offset:57344
	ds_read_b128 v[250:253], v206 offset:49152
	s_waitcnt lgkmcnt(6)
	v_mfma_f32_32x32x16_bf16 v[114:129], v[178:181], v[174:177], 0
	ds_read_b128 v[178:181], v206 offset:57344
	v_add_f32_e32 v16, 0, v154
	v_add_f32_e32 v16, v158, v16
	v_add_f32_e32 v16, v155, v16
	v_add_f32_e32 v16, v159, v16
	v_add_f32_e32 v16, v156, v16
	s_waitcnt lgkmcnt(6)
	v_mfma_f32_32x32x16_bf16 v[98:113], v[216:219], v[174:177], 0
	ds_read_b128 v[216:219], v198 offset:49280
	v_add_f32_e32 v16, v160, v16
	v_add_f32_e32 v16, v157, v16
	v_add_f32_e32 v16, v161, v16
	v_add_f32_e32 v16, v146, v16
	s_waitcnt lgkmcnt(6)
	v_mfma_f32_32x32x16_bf16 v[114:129], v[228:231], v[170:173], v[114:129]
	ds_read_b128 v[228:231], v191 offset:4096
	v_add_f32_e32 v16, v150, v16
	v_add_f32_e32 v16, v147, v16
	v_add_f32_e32 v16, v151, v16
	v_exp_f32_e32 v2, v144
	s_waitcnt lgkmcnt(6)
	v_mfma_f32_32x32x16_bf16 v[98:113], v[232:235], v[170:173], v[98:113]
	ds_read_b128 v[232:235], v198 offset:57472
	v_add_f32_e32 v16, v148, v16
	v_exp_f32_e32 v4, v145
	v_add_f32_e32 v16, v152, v16
	v_exp_f32_e32 v5, v140
	s_waitcnt lgkmcnt(6)
	v_mfma_f32_32x32x16_bf16 v[114:129], v[238:241], v[166:169], v[114:129]
	ds_read_b128 v[238:241], v204 offset:49280
	v_add_f32_e32 v16, v149, v16
	v_exp_f32_e32 v6, v141
	v_add_f32_e32 v16, v153, v16
	v_exp_f32_e32 v7, v138
	s_waitcnt lgkmcnt(6)
	v_mfma_f32_32x32x16_bf16 v[98:113], v[242:245], v[166:169], v[98:113]
	ds_read_b128 v[242:245], v191 offset:5120
	v_add_f32_e32 v16, v2, v16
	v_exp_f32_e32 v8, v139
	v_add_f32_e32 v16, v4, v16
	v_exp_f32_e32 v9, v132
	s_waitcnt lgkmcnt(6)
	v_mfma_f32_32x32x16_bf16 v[114:129], v[250:253], v[162:165], v[114:129]
	ds_read_b128 v[250:253], v204 offset:57472
	v_add_f32_e32 v16, v5, v16
	v_exp_f32_e32 v10, v133
	v_add_f32_e32 v16, v6, v16
	v_exp_f32_e32 v11, v130
	s_waitcnt lgkmcnt(6)
	v_mfma_f32_32x32x16_bf16 v[98:113], v[178:181], v[162:165], v[98:113]
	ds_read_b128 v[178:181], v205 offset:49280
	v_add_f32_e32 v16, v7, v16
	v_exp_f32_e32 v12, v131
	v_add_f32_e32 v16, v8, v16
	v_exp_f32_e32 v13, v142
	s_waitcnt lgkmcnt(5)
	v_mfma_f32_32x32x16_bf16 v[114:129], v[216:219], v[228:231], v[114:129]
	ds_read_b128 v[216:219], v191 offset:6144
	v_add_f32_e32 v16, v9, v16
	v_exp_f32_e32 v14, v143
	v_add_f32_e32 v16, v10, v16
	v_exp_f32_e32 v15, v136
	s_waitcnt lgkmcnt(5)
	v_mfma_f32_32x32x16_bf16 v[98:113], v[232:235], v[228:231], v[98:113]
	ds_read_b128 v[232:235], v205 offset:57472
	ds_read_b128 v[228:231], v206 offset:49280
	v_add_f32_e32 v16, v11, v16
	v_exp_f32_e32 v19, v137
	v_add_f32_e32 v16, v12, v16
	v_exp_f32_e32 v32, v134
	s_waitcnt lgkmcnt(5)
	v_mfma_f32_32x32x16_bf16 v[114:129], v[238:241], v[242:245], v[114:129]
	ds_read_b128 v[238:241], v191 offset:7168
	v_add_f32_e32 v16, v13, v16
	v_exp_f32_e32 v33, v135
	v_add_f32_e32 v16, v14, v16
	v_add_f32_e32 v16, v15, v16
	s_waitcnt lgkmcnt(5)
	v_mfma_f32_32x32x16_bf16 v[98:113], v[250:253], v[242:245], v[98:113]
	ds_read_b128 v[250:253], v206 offset:57472
	v_add_f32_e32 v16, v19, v16
	v_add_f32_e32 v16, v32, v16
	v_add_f32_e32 v16, v33, v16
	v_mov_b32_e32 v17, v16
	s_waitcnt lgkmcnt(4)
	v_mfma_f32_32x32x16_bf16 v[114:129], v[178:181], v[216:219], v[114:129]
	v_cvt_pk_bf16_f32 v20, v154, v158
	v_cvt_pk_bf16_f32 v21, v155, v159
	v_cvt_pk_bf16_f32 v22, v156, v160
	v_cvt_pk_bf16_f32 v23, v157, v161
	s_waitcnt lgkmcnt(3)
	v_mfma_f32_32x32x16_bf16 v[98:113], v[232:235], v[216:219], v[98:113]
	v_cvt_pk_bf16_f32 v24, v146, v150
	v_cvt_pk_bf16_f32 v25, v147, v151
	v_cvt_pk_bf16_f32 v26, v148, v152
	v_cvt_pk_bf16_f32 v27, v149, v153
	s_waitcnt lgkmcnt(1)
	v_mfma_f32_32x32x16_bf16 v[114:129], v[228:231], v[238:241], v[114:129]
	v_cvt_pk_bf16_f32 v28, v2, v4
	v_cvt_pk_bf16_f32 v29, v5, v6
	v_cvt_pk_bf16_f32 v30, v7, v8
	v_cvt_pk_bf16_f32 v31, v9, v10
	s_waitcnt lgkmcnt(0)
	v_mfma_f32_32x32x16_bf16 v[98:113], v[250:253], v[238:241], v[98:113]
	v_cvt_pk_bf16_f32 v130, v11, v12
	v_cvt_pk_bf16_f32 v131, v13, v14
	v_cvt_pk_bf16_f32 v132, v15, v19
	v_cvt_pk_bf16_f32 v133, v32, v33
	s_branch .LBB0_3238

.LBB0_3237:
	v_mov_b32_e32 v32, v18
	v_mov_b32_e32 v33, v18
	v_mov_b32_e32 v19, v18
	v_mov_b32_e32 v20, v18
	v_mov_b32_e32 v21, v18
	v_mov_b32_e32 v22, v18
	v_mov_b32_e32 v23, v18
	v_mov_b32_e32 v24, v18
	v_mov_b32_e32 v25, v18
	v_mov_b32_e32 v26, v18
	v_mov_b32_e32 v27, v18
	v_mov_b32_e32 v28, v18
	v_mov_b32_e32 v29, v18
	v_mov_b32_e32 v30, v18
	v_mov_b32_e32 v31, v18
	v_mov_b64_e32 v[128:129], v[32:33]
	v_mov_b64_e32 v[112:113], v[32:33]
	v_mov_b64_e32 v[126:127], v[30:31]
	v_mov_b64_e32 v[124:125], v[28:29]
	v_mov_b64_e32 v[122:123], v[26:27]
	v_mov_b64_e32 v[120:121], v[24:25]
	v_mov_b64_e32 v[118:119], v[22:23]
	v_mov_b64_e32 v[116:117], v[20:21]
	v_mov_b64_e32 v[114:115], v[18:19]
	v_mov_b64_e32 v[110:111], v[30:31]
	v_mov_b64_e32 v[108:109], v[28:29]
	v_mov_b64_e32 v[106:107], v[26:27]
	v_mov_b64_e32 v[104:105], v[24:25]
	v_mov_b64_e32 v[102:103], v[22:23]
	v_mov_b64_e32 v[100:101], v[20:21]
	v_mov_b64_e32 v[98:99], v[18:19]
	v_add_f32_e32 v16, 0, v154
	v_add_f32_e32 v16, v158, v16
	v_add_f32_e32 v16, v155, v16
	v_add_f32_e32 v16, v159, v16
	v_add_f32_e32 v16, v156, v16
	v_add_f32_e32 v16, v160, v16
	v_add_f32_e32 v16, v157, v16
	v_add_f32_e32 v16, v161, v16
	v_add_f32_e32 v16, v146, v16
	v_add_f32_e32 v16, v150, v16
	v_add_f32_e32 v16, v147, v16
	v_add_f32_e32 v16, v151, v16
	v_exp_f32_e32 v2, v144
	v_add_f32_e32 v16, v148, v16
	v_exp_f32_e32 v4, v145
	v_add_f32_e32 v16, v152, v16
	v_exp_f32_e32 v5, v140
	v_add_f32_e32 v16, v149, v16
	v_exp_f32_e32 v6, v141
	v_add_f32_e32 v16, v153, v16
	v_exp_f32_e32 v7, v138
	v_add_f32_e32 v16, v2, v16
	v_exp_f32_e32 v8, v139
	v_add_f32_e32 v16, v4, v16
	v_exp_f32_e32 v9, v132
	v_add_f32_e32 v16, v5, v16
	v_exp_f32_e32 v10, v133
	v_add_f32_e32 v16, v6, v16
	v_exp_f32_e32 v11, v130
	v_add_f32_e32 v16, v7, v16
	v_exp_f32_e32 v12, v131
	v_add_f32_e32 v16, v8, v16
	v_exp_f32_e32 v13, v142
	v_add_f32_e32 v16, v9, v16
	v_exp_f32_e32 v14, v143
	v_add_f32_e32 v16, v10, v16
	v_exp_f32_e32 v15, v136
	v_add_f32_e32 v16, v11, v16
	v_exp_f32_e32 v19, v137
	v_add_f32_e32 v16, v12, v16
	v_exp_f32_e32 v32, v134
	v_add_f32_e32 v16, v13, v16
	v_exp_f32_e32 v33, v135
	v_add_f32_e32 v16, v14, v16
	v_add_f32_e32 v16, v15, v16
	v_add_f32_e32 v16, v19, v16
	v_add_f32_e32 v16, v32, v16
	v_add_f32_e32 v16, v33, v16
	v_mov_b32_e32 v17, v16
	v_cvt_pk_bf16_f32 v20, v154, v158
	v_cvt_pk_bf16_f32 v21, v155, v159
	v_cvt_pk_bf16_f32 v22, v156, v160
	v_cvt_pk_bf16_f32 v23, v157, v161
	v_cvt_pk_bf16_f32 v24, v146, v150
	v_cvt_pk_bf16_f32 v25, v147, v151
	v_cvt_pk_bf16_f32 v26, v148, v152
	v_cvt_pk_bf16_f32 v27, v149, v153
	v_cvt_pk_bf16_f32 v28, v2, v4
	v_cvt_pk_bf16_f32 v29, v5, v6
	v_cvt_pk_bf16_f32 v30, v7, v8
	v_cvt_pk_bf16_f32 v31, v9, v10
	v_cvt_pk_bf16_f32 v130, v11, v12
	v_cvt_pk_bf16_f32 v131, v13, v14
	v_cvt_pk_bf16_f32 v132, v15, v19
	v_cvt_pk_bf16_f32 v133, v32, v33
.LBB0_3238:
	s_add_i32 s2, s73, 2
	s_nop 0
	v_permlane32_swap_b32_e32 v16, v17
	v_permlane32_swap_b32_e32 v20, v22
	v_permlane32_swap_b32_e32 v21, v23
	v_permlane32_swap_b32_e32 v24, v26
	v_permlane32_swap_b32_e32 v25, v27
	v_permlane32_swap_b32_e32 v28, v30
	v_permlane32_swap_b32_e32 v29, v31
	v_permlane32_swap_b32_e32 v130, v132
	v_permlane32_swap_b32_e32 v131, v133
	s_and_b32 s12, s2, 0x7ffffffc
	s_lshr_b32 s92, s78, s12
	s_lshl_b32 s12, s92, 8
	s_and_b32 s12, s12, 0xf00
	s_and_b32 s94, s72, 0xc0
	s_or_b32 s12, s12, s94
	v_or_b32_e32 v2, s12, v227
	v_or_b32_e32 v6, s12, v1
	v_mul_u32_u24_e32 v2, 0x1800, v2
	v_mul_u32_u24_e32 v6, 0x1800, v6
	v_lshlrev_b32_e32 v2, 1, v2
	v_lshlrev_b32_e32 v12, 1, v6
	v_mov_b32_e32 v13, v3
	v_lshl_add_u64 v[4:5], v[192:193], 0, v[2:3]
	v_lshl_add_u64 v[8:9], v[192:193], 0, v[12:13]
	v_lshl_add_u64 v[14:15], v[194:195], 0, v[2:3]
	global_load_dwordx4 v[4:7], v[4:5], off
	s_nop 0
	global_load_dwordx4 v[8:11], v[8:9], off
	v_lshl_add_u64 v[32:33], v[194:195], 0, v[12:13]
	global_load_dwordx4 v[12:15], v[14:15], off
	s_nop 0
	global_load_dwordx4 v[178:181], v[32:33], off
	s_and_b32 s12, s73, -4
	s_lshr_b32 s12, s78, s12
	s_and_b32 s16, s12, 15
	s_cmp_lg_u32 s16, s80
	s_mov_b64 s[14:15], -1
	s_cbranch_scc0 .LBB0_3243
	s_lshr_b32 s12, s83, s16
	s_bitcmp1_b32 s12, 0
	s_cselect_b64 s[12:13], -1, 0
	s_cbranch_execz .LBB0_3244

.LBB0_3264:
	ds_read_b128 v[218:221], v198 offset:32768
	ds_read_b128 v[228:231], v198 offset:40960
	ds_read_b128 v[232:235], v204 offset:32768
	ds_read_b128 v[236:239], v204 offset:40960
	ds_read_b128 v[240:243], v205 offset:32768
	ds_read_b128 v[244:247], v205 offset:40960
	ds_read_b128 v[250:253], v206 offset:32768
	s_waitcnt lgkmcnt(6)
	v_mfma_f32_32x32x16_bf16 v[114:129], v[218:221], v[174:177], 0
	ds_read_b128 v[218:221], v206 offset:40960
	v_add_f32_e32 v19, 0, v142
	v_add_f32_e32 v19, v144, v19
	v_add_f32_e32 v19, v140, v19
	v_add_f32_e32 v19, v143, v19
	v_add_f32_e32 v19, v138, v19
	s_waitcnt lgkmcnt(6)
	v_mfma_f32_32x32x16_bf16 v[98:113], v[228:231], v[174:177], 0
	ds_read_b128 v[228:231], v198 offset:32896
	v_add_f32_e32 v19, v141, v19
	v_add_f32_e32 v19, v137, v19
	v_add_f32_e32 v19, v139, v19
	v_add_f32_e32 v19, v134, v19
	s_waitcnt lgkmcnt(6)
	v_mfma_f32_32x32x16_bf16 v[114:129], v[232:235], v[170:173], v[114:129]
	ds_read_b128 v[232:235], v191 offset:4096
	v_add_f32_e32 v19, v136, v19
	v_add_f32_e32 v19, v132, v19
	v_add_f32_e32 v19, v135, v19
	v_exp_f32_e32 v28, v146
	s_waitcnt lgkmcnt(6)
	v_mfma_f32_32x32x16_bf16 v[98:113], v[236:239], v[170:173], v[98:113]
	ds_read_b128 v[236:239], v198 offset:41088
	v_add_f32_e32 v19, v130, v19
	v_exp_f32_e32 v29, v147
	v_add_f32_e32 v19, v133, v19
	v_exp_f32_e32 v30, v148
	s_waitcnt lgkmcnt(6)
	v_mfma_f32_32x32x16_bf16 v[114:129], v[240:243], v[166:169], v[114:129]
	ds_read_b128 v[240:243], v204 offset:32896
	v_add_f32_e32 v19, v2, v19
	v_exp_f32_e32 v31, v149
	v_add_f32_e32 v19, v131, v19
	v_exp_f32_e32 v33, v150
	s_waitcnt lgkmcnt(6)
	v_mfma_f32_32x32x16_bf16 v[98:113], v[244:247], v[166:169], v[98:113]
	ds_read_b128 v[244:247], v191 offset:5120
	v_add_f32_e32 v19, v28, v19
	v_exp_f32_e32 v146, v151
	v_add_f32_e32 v19, v29, v19
	v_exp_f32_e32 v147, v152
	s_waitcnt lgkmcnt(6)
	v_mfma_f32_32x32x16_bf16 v[114:129], v[250:253], v[162:165], v[114:129]
	ds_read_b128 v[250:253], v204 offset:41088
	v_add_f32_e32 v19, v30, v19
	v_exp_f32_e32 v148, v153
	v_add_f32_e32 v19, v31, v19
	v_exp_f32_e32 v149, v154
	s_waitcnt lgkmcnt(6)
	v_mfma_f32_32x32x16_bf16 v[98:113], v[218:221], v[162:165], v[98:113]
	ds_read_b128 v[218:221], v205 offset:32896
	v_add_f32_e32 v19, v33, v19
	v_exp_f32_e32 v150, v155
	v_add_f32_e32 v19, v146, v19
	v_exp_f32_e32 v151, v156
	s_waitcnt lgkmcnt(5)
	v_mfma_f32_32x32x16_bf16 v[114:129], v[228:231], v[232:235], v[114:129]
	ds_read_b128 v[228:231], v191 offset:6144
	v_add_f32_e32 v19, v147, v19
	v_exp_f32_e32 v152, v157
	v_add_f32_e32 v19, v148, v19
	v_exp_f32_e32 v153, v158
	s_waitcnt lgkmcnt(5)
	v_mfma_f32_32x32x16_bf16 v[98:113], v[236:239], v[232:235], v[98:113]
	ds_read_b128 v[236:239], v205 offset:41088
	ds_read_b128 v[232:235], v206 offset:32896
	v_add_f32_e32 v19, v149, v19
	v_exp_f32_e32 v154, v159
	v_add_f32_e32 v19, v150, v19
	v_exp_f32_e32 v155, v160
	s_waitcnt lgkmcnt(5)
	v_mfma_f32_32x32x16_bf16 v[114:129], v[240:243], v[244:247], v[114:129]
	ds_read_b128 v[240:243], v191 offset:7168
	v_add_f32_e32 v19, v151, v19
	v_exp_f32_e32 v145, v145
	v_add_f32_e32 v19, v152, v19
	v_add_f32_e32 v19, v153, v19
	s_waitcnt lgkmcnt(5)
	v_mfma_f32_32x32x16_bf16 v[98:113], v[250:253], v[244:247], v[98:113]
	ds_read_b128 v[250:253], v206 offset:41088
	v_add_f32_e32 v19, v154, v19
	v_add_f32_e32 v19, v155, v19
	v_add_f32_e32 v19, v145, v19
	v_mov_b32_e32 v32, v19
	s_waitcnt lgkmcnt(4)
	v_mfma_f32_32x32x16_bf16 v[114:129], v[218:221], v[228:231], v[114:129]
	v_cvt_pk_bf16_f32 v20, v142, v144
	v_cvt_pk_bf16_f32 v21, v140, v143
	v_cvt_pk_bf16_f32 v22, v138, v141
	v_cvt_pk_bf16_f32 v23, v137, v139
	s_waitcnt lgkmcnt(3)
	v_mfma_f32_32x32x16_bf16 v[98:113], v[236:239], v[228:231], v[98:113]
	v_cvt_pk_bf16_f32 v24, v134, v136
	v_cvt_pk_bf16_f32 v25, v132, v135
	v_cvt_pk_bf16_f32 v26, v130, v133
	v_cvt_pk_bf16_f32 v27, v2, v131
	s_waitcnt lgkmcnt(1)
	v_mfma_f32_32x32x16_bf16 v[114:129], v[232:235], v[240:243], v[114:129]
	v_cvt_pk_bf16_f32 v28, v28, v29
	v_cvt_pk_bf16_f32 v29, v30, v31
	v_cvt_pk_bf16_f32 v30, v33, v146
	v_cvt_pk_bf16_f32 v31, v147, v148
	s_waitcnt lgkmcnt(0)
	v_mfma_f32_32x32x16_bf16 v[98:113], v[250:253], v[240:243], v[98:113]
	v_cvt_pk_bf16_f32 v130, v149, v150
	v_cvt_pk_bf16_f32 v131, v151, v152
	v_cvt_pk_bf16_f32 v132, v153, v154
	v_cvt_pk_bf16_f32 v133, v155, v145
	s_branch .LBB0_3268

.LBB0_3267:
	v_mov_b32_e32 v32, v18
	v_mov_b32_e32 v33, v18
	v_mov_b32_e32 v19, v18
	v_mov_b32_e32 v20, v18
	v_mov_b32_e32 v21, v18
	v_mov_b32_e32 v22, v18
	v_mov_b32_e32 v23, v18
	v_mov_b32_e32 v24, v18
	v_mov_b32_e32 v25, v18
	v_mov_b32_e32 v26, v18
	v_mov_b32_e32 v27, v18
	v_mov_b32_e32 v28, v18
	v_mov_b32_e32 v29, v18
	v_mov_b32_e32 v30, v18
	v_mov_b32_e32 v31, v18
	v_mov_b64_e32 v[128:129], v[32:33]
	v_mov_b64_e32 v[112:113], v[32:33]
	v_mov_b64_e32 v[126:127], v[30:31]
	v_mov_b64_e32 v[124:125], v[28:29]
	v_mov_b64_e32 v[122:123], v[26:27]
	v_mov_b64_e32 v[120:121], v[24:25]
	v_mov_b64_e32 v[118:119], v[22:23]
	v_mov_b64_e32 v[116:117], v[20:21]
	v_mov_b64_e32 v[114:115], v[18:19]
	v_mov_b64_e32 v[110:111], v[30:31]
	v_mov_b64_e32 v[108:109], v[28:29]
	v_mov_b64_e32 v[106:107], v[26:27]
	v_mov_b64_e32 v[104:105], v[24:25]
	v_mov_b64_e32 v[102:103], v[22:23]
	v_mov_b64_e32 v[100:101], v[20:21]
	v_mov_b64_e32 v[98:99], v[18:19]
	v_add_f32_e32 v19, 0, v142
	v_add_f32_e32 v19, v144, v19
	v_add_f32_e32 v19, v140, v19
	v_add_f32_e32 v19, v143, v19
	v_add_f32_e32 v19, v138, v19
	v_add_f32_e32 v19, v141, v19
	v_add_f32_e32 v19, v137, v19
	v_add_f32_e32 v19, v139, v19
	v_add_f32_e32 v19, v134, v19
	v_add_f32_e32 v19, v136, v19
	v_add_f32_e32 v19, v132, v19
	v_add_f32_e32 v19, v135, v19
	v_exp_f32_e32 v28, v146
	v_add_f32_e32 v19, v130, v19
	v_exp_f32_e32 v29, v147
	v_add_f32_e32 v19, v133, v19
	v_exp_f32_e32 v30, v148
	v_add_f32_e32 v19, v2, v19
	v_exp_f32_e32 v31, v149
	v_add_f32_e32 v19, v131, v19
	v_exp_f32_e32 v33, v150
	v_add_f32_e32 v19, v28, v19
	v_exp_f32_e32 v146, v151
	v_add_f32_e32 v19, v29, v19
	v_exp_f32_e32 v147, v152
	v_add_f32_e32 v19, v30, v19
	v_exp_f32_e32 v148, v153
	v_add_f32_e32 v19, v31, v19
	v_exp_f32_e32 v149, v154
	v_add_f32_e32 v19, v33, v19
	v_exp_f32_e32 v150, v155
	v_add_f32_e32 v19, v146, v19
	v_exp_f32_e32 v151, v156
	v_add_f32_e32 v19, v147, v19
	v_exp_f32_e32 v152, v157
	v_add_f32_e32 v19, v148, v19
	v_exp_f32_e32 v153, v158
	v_add_f32_e32 v19, v149, v19
	v_exp_f32_e32 v154, v159
	v_add_f32_e32 v19, v150, v19
	v_exp_f32_e32 v155, v160
	v_add_f32_e32 v19, v151, v19
	v_exp_f32_e32 v145, v145
	v_add_f32_e32 v19, v152, v19
	v_add_f32_e32 v19, v153, v19
	v_add_f32_e32 v19, v154, v19
	v_add_f32_e32 v19, v155, v19
	v_add_f32_e32 v19, v145, v19
	v_mov_b32_e32 v32, v19
	v_cvt_pk_bf16_f32 v20, v142, v144
	v_cvt_pk_bf16_f32 v21, v140, v143
	v_cvt_pk_bf16_f32 v22, v138, v141
	v_cvt_pk_bf16_f32 v23, v137, v139
	v_cvt_pk_bf16_f32 v24, v134, v136
	v_cvt_pk_bf16_f32 v25, v132, v135
	v_cvt_pk_bf16_f32 v26, v130, v133
	v_cvt_pk_bf16_f32 v27, v2, v131
	v_cvt_pk_bf16_f32 v28, v28, v29
	v_cvt_pk_bf16_f32 v29, v30, v31
	v_cvt_pk_bf16_f32 v30, v33, v146
	v_cvt_pk_bf16_f32 v31, v147, v148
	v_cvt_pk_bf16_f32 v130, v149, v150
	v_cvt_pk_bf16_f32 v131, v151, v152
	v_cvt_pk_bf16_f32 v132, v153, v154
	v_cvt_pk_bf16_f32 v133, v155, v145
.LBB0_3268:
	s_nop 1
	v_permlane32_swap_b32_e32 v19, v32
	v_permlane32_swap_b32_e32 v20, v22
	v_permlane32_swap_b32_e32 v21, v23
	v_permlane32_swap_b32_e32 v24, v26
	v_permlane32_swap_b32_e32 v25, v27
	v_permlane32_swap_b32_e32 v28, v30
	v_permlane32_swap_b32_e32 v29, v31
	v_permlane32_swap_b32_e32 v130, v132
	v_permlane32_swap_b32_e32 v131, v133
	s_add_i32 s12, s73, 3
	s_cmp_lt_u32 s12, s79
	s_cselect_b64 s[70:71], -1, 0
	s_cmp_ge_u32 s12, s79
	s_cbranch_scc1 .LBB0_3270
	s_and_b32 s12, s12, 0x7ffffffc
	s_lshr_b32 s12, s78, s12
	s_lshl_b32 s12, s12, 8
	s_add_i32 s13, s72, 64
	s_and_b32 s12, s12, 0xf00
	s_and_b32 s13, s13, 0xc0
	s_or_b32 s12, s12, s13
	v_or_b32_e32 v2, s12, v227
	v_or_b32_e32 v6, s12, v1
	v_mul_u32_u24_e32 v2, 0x1800, v2
	v_mul_u32_u24_e32 v6, 0x1800, v6
	v_lshlrev_b32_e32 v2, 1, v2
	v_lshlrev_b32_e32 v12, 1, v6
	v_mov_b32_e32 v13, v3
	v_lshl_add_u64 v[4:5], v[192:193], 0, v[2:3]
	v_lshl_add_u64 v[8:9], v[192:193], 0, v[12:13]
	v_lshl_add_u64 v[14:15], v[194:195], 0, v[2:3]
	global_load_dwordx4 v[4:7], v[4:5], off
	s_nop 0
	global_load_dwordx4 v[8:11], v[8:9], off
	v_lshl_add_u64 v[134:135], v[194:195], 0, v[12:13]
	global_load_dwordx4 v[12:15], v[14:15], off
	s_nop 0
	global_load_dwordx4 v[178:181], v[134:135], off
